# plus DSA score-row loads rewritten: saddr loads with immediate offsets straight into the key registers, 4 keys per wait
# speedup vs baseline: 1.0025x; 1.0025x over previous
; __device__ __forceinline__ void dsa2_unit(LAS unsigned char* lds, const bf16* PROJ, const bf16* KIDX, const bf16* KVN, bf16* OLAT, float* sbuf, int b, int t0, int tid) {
;     ...
;         asm volatile("s_waitcnt vmcnt(0)" ::: "memory");
;         __syncthreads();
;         const int n = t + 1, nreg = (n + 63) >> 6; const float* sr = sbuf + (size_t)wave * 8192;
;         unsigned kk[128];
;     ...
;         for (int repk = 0; repk < DUP_KK; ++repk)
; #pragma unroll
;         for (int gI = 0; gI < 4; ++gI) {
;             if (gI * 32 < nreg) {
;                 float fv[32];
; #pragma unroll
;                 for (int i = 0; i < 32; ++i) { const int key = lane + 64 * (gI * 32 + i); fv[i] = __hip_atomic_load(sr + (key < n ? key : n - 1), __ATOMIC_RELAXED, __HIP_MEMORY_SCOPE_AGENT); }
; #pragma unroll
;                 for (int i = 0; i < 32; ++i) { const int key = lane + 64 * (gI * 32 + i); kk[gI * 32 + i] = key < n ? __builtin_bit_cast(unsigned, fv[i]) : 0u; }
;             } else {
; #pragma unroll
;                 for (int i = 0; i < 32; ++i) kk[gI * 32 + i] = 0u;
;             }
;         }
.LBB0_720:
	s_add_i32 s1, s58, 64
	s_ashr_i32 s49, s1, 6
	s_ashr_i32 s1, s0, 31
	s_waitcnt vmcnt(0)
	s_lshl_b64 s[0:1], s[0:1], 15
	s_cmp_gt_i32 s49, 0
	s_cselect_b64 s[8:9], -1, 0
	s_cmp_lt_i32 s49, 1
	s_waitcnt vmcnt(0)
	v_lshl_add_u64 v[0:1], v[140:141], 0, s[0:1]
	s_barrier
	s_cbranch_scc1 .LBB0_722
	v_readfirstlane_b32 s2, v0
	v_readfirstlane_b32 s3, v1
	v_lshlrev_b32_e32 v2, 2, v129
	s_nop 3
	s_add_i32 s4, s58, 1
	s_nop 1
	global_load_dword v166, v2, s[2:3] sc1
	global_load_dword v165, v2, s[2:3] offset:256 sc1
	global_load_dword v164, v2, s[2:3] offset:512 sc1
	global_load_dword v163, v2, s[2:3] offset:768 sc1
	global_load_dword v162, v2, s[2:3] offset:1024 sc1
	global_load_dword v161, v2, s[2:3] offset:1280 sc1
	global_load_dword v160, v2, s[2:3] offset:1536 sc1
	global_load_dword v159, v2, s[2:3] offset:1792 sc1
	global_load_dword v158, v2, s[2:3] offset:2048 sc1
	global_load_dword v157, v2, s[2:3] offset:2304 sc1
	global_load_dword v155, v2, s[2:3] offset:2560 sc1
	global_load_dword v154, v2, s[2:3] offset:2816 sc1
	global_load_dword v153, v2, s[2:3] offset:3072 sc1
	global_load_dword v152, v2, s[2:3] offset:3328 sc1
	global_load_dword v151, v2, s[2:3] offset:3584 sc1
	global_load_dword v149, v2, s[2:3] offset:3840 sc1
	s_add_u32 s2, s2, 0x1000
	s_addc_u32 s3, s3, 0
	global_load_dword v148, v2, s[2:3] sc1
	global_load_dword v147, v2, s[2:3] offset:256 sc1
	global_load_dword v146, v2, s[2:3] offset:512 sc1
	global_load_dword v145, v2, s[2:3] offset:768 sc1
	global_load_dword v144, v2, s[2:3] offset:1024 sc1
	global_load_dword v143, v2, s[2:3] offset:1280 sc1
	global_load_dword v142, v2, s[2:3] offset:1536 sc1
	global_load_dword v141, v2, s[2:3] offset:1792 sc1
	global_load_dword v140, v2, s[2:3] offset:2048 sc1
	global_load_dword v139, v2, s[2:3] offset:2304 sc1
	global_load_dword v137, v2, s[2:3] offset:2560 sc1
	global_load_dword v136, v2, s[2:3] offset:2816 sc1
	global_load_dword v134, v2, s[2:3] offset:3072 sc1
	global_load_dword v132, v2, s[2:3] offset:3328 sc1
	global_load_dword v130, v2, s[2:3] offset:3584 sc1
	global_load_dword v126, v2, s[2:3] offset:3840 sc1
	v_cmp_gt_i32_e64 s[10:11], s4, v129
	s_sub_i32 s4, s4, 64
	v_cmp_gt_i32_e64 s[12:13], s4, v129
	s_sub_i32 s4, s4, 64
	v_cmp_gt_i32_e64 s[14:15], s4, v129
	s_sub_i32 s4, s4, 64
	v_cmp_gt_i32_e32 vcc, s4, v129
	s_sub_i32 s4, s4, 64
	s_waitcnt vmcnt(28)
	v_cndmask_b32_e64 v166, 0, v166, s[10:11]
	v_cndmask_b32_e64 v165, 0, v165, s[12:13]
	v_cndmask_b32_e64 v164, 0, v164, s[14:15]
	v_cndmask_b32_e32 v163, 0, v163, vcc
	v_cmp_gt_i32_e64 s[10:11], s4, v129
	s_sub_i32 s4, s4, 64
	v_cmp_gt_i32_e64 s[12:13], s4, v129
	s_sub_i32 s4, s4, 64
	v_cmp_gt_i32_e64 s[14:15], s4, v129
	s_sub_i32 s4, s4, 64
	v_cmp_gt_i32_e32 vcc, s4, v129
	s_sub_i32 s4, s4, 64
	s_waitcnt vmcnt(24)
	v_cndmask_b32_e64 v162, 0, v162, s[10:11]
	v_cndmask_b32_e64 v161, 0, v161, s[12:13]
	v_cndmask_b32_e64 v160, 0, v160, s[14:15]
	v_cndmask_b32_e32 v159, 0, v159, vcc
	v_cmp_gt_i32_e64 s[10:11], s4, v129
	s_sub_i32 s4, s4, 64
	v_cmp_gt_i32_e64 s[12:13], s4, v129
	s_sub_i32 s4, s4, 64
	v_cmp_gt_i32_e64 s[14:15], s4, v129
	s_sub_i32 s4, s4, 64
	v_cmp_gt_i32_e32 vcc, s4, v129
	s_sub_i32 s4, s4, 64
	s_waitcnt vmcnt(20)
	v_cndmask_b32_e64 v158, 0, v158, s[10:11]
	v_cndmask_b32_e64 v157, 0, v157, s[12:13]
	v_cndmask_b32_e64 v155, 0, v155, s[14:15]
	v_cndmask_b32_e32 v154, 0, v154, vcc
	v_cmp_gt_i32_e64 s[10:11], s4, v129
	s_sub_i32 s4, s4, 64
	v_cmp_gt_i32_e64 s[12:13], s4, v129
	s_sub_i32 s4, s4, 64
	v_cmp_gt_i32_e64 s[14:15], s4, v129
	s_sub_i32 s4, s4, 64
	v_cmp_gt_i32_e32 vcc, s4, v129
	s_sub_i32 s4, s4, 64
	s_waitcnt vmcnt(16)
	v_cndmask_b32_e64 v153, 0, v153, s[10:11]
	v_cndmask_b32_e64 v152, 0, v152, s[12:13]
	v_cndmask_b32_e64 v151, 0, v151, s[14:15]
	v_cndmask_b32_e32 v149, 0, v149, vcc
	v_cmp_gt_i32_e64 s[10:11], s4, v129
	s_sub_i32 s4, s4, 64
	v_cmp_gt_i32_e64 s[12:13], s4, v129
	s_sub_i32 s4, s4, 64
	v_cmp_gt_i32_e64 s[14:15], s4, v129
	s_sub_i32 s4, s4, 64
	v_cmp_gt_i32_e32 vcc, s4, v129
	s_sub_i32 s4, s4, 64
	s_waitcnt vmcnt(12)
	v_cndmask_b32_e64 v148, 0, v148, s[10:11]
	v_cndmask_b32_e64 v147, 0, v147, s[12:13]
	v_cndmask_b32_e64 v146, 0, v146, s[14:15]
	v_cndmask_b32_e32 v145, 0, v145, vcc
	v_cmp_gt_i32_e64 s[10:11], s4, v129
	s_sub_i32 s4, s4, 64
	v_cmp_gt_i32_e64 s[12:13], s4, v129
	s_sub_i32 s4, s4, 64
	v_cmp_gt_i32_e64 s[14:15], s4, v129
	s_sub_i32 s4, s4, 64
	v_cmp_gt_i32_e32 vcc, s4, v129
	s_sub_i32 s4, s4, 64
	s_waitcnt vmcnt(8)
	v_cndmask_b32_e64 v144, 0, v144, s[10:11]
	v_cndmask_b32_e64 v143, 0, v143, s[12:13]
	v_cndmask_b32_e64 v142, 0, v142, s[14:15]
	v_cndmask_b32_e32 v141, 0, v141, vcc
	v_cmp_gt_i32_e64 s[10:11], s4, v129
	s_sub_i32 s4, s4, 64
	v_cmp_gt_i32_e64 s[12:13], s4, v129
	s_sub_i32 s4, s4, 64
	v_cmp_gt_i32_e64 s[14:15], s4, v129
	s_sub_i32 s4, s4, 64
	v_cmp_gt_i32_e32 vcc, s4, v129
	s_sub_i32 s4, s4, 64
	s_waitcnt vmcnt(4)
	v_cndmask_b32_e64 v140, 0, v140, s[10:11]
	v_cndmask_b32_e64 v139, 0, v139, s[12:13]
	v_cndmask_b32_e64 v137, 0, v137, s[14:15]
	v_cndmask_b32_e32 v136, 0, v136, vcc
	v_cmp_gt_i32_e64 s[10:11], s4, v129
	s_sub_i32 s4, s4, 64
	v_cmp_gt_i32_e64 s[12:13], s4, v129
	s_sub_i32 s4, s4, 64
	v_cmp_gt_i32_e64 s[14:15], s4, v129
	s_sub_i32 s4, s4, 64
	v_cmp_gt_i32_e32 vcc, s4, v129
	s_sub_i32 s4, s4, 64
	s_waitcnt vmcnt(0)
	v_cndmask_b32_e64 v134, 0, v134, s[10:11]
	v_cndmask_b32_e64 v132, 0, v132, s[12:13]
	v_cndmask_b32_e64 v130, 0, v130, s[14:15]
	v_cndmask_b32_e32 v126, 0, v126, vcc
	s_branch .LBB0_723

; __device__ __forceinline__ void dsa2_unit(LAS unsigned char* lds, const bf16* PROJ, const bf16* KIDX, const bf16* KVN, bf16* OLAT, float* sbuf, int b, int t0, int tid) {
;     ...
;         for (int repk = 0; repk < DUP_KK; ++repk)
; #pragma unroll
;         for (int gI = 0; gI < 4; ++gI) {
;             if (gI * 32 < nreg) {
;                 float fv[32];
; #pragma unroll
;                 for (int i = 0; i < 32; ++i) { const int key = lane + 64 * (gI * 32 + i); fv[i] = __hip_atomic_load(sr + (key < n ? key : n - 1), __ATOMIC_RELAXED, __HIP_MEMORY_SCOPE_AGENT); }
; #pragma unroll
;                 for (int i = 0; i < 32; ++i) { const int key = lane + 64 * (gI * 32 + i); kk[gI * 32 + i] = key < n ? __builtin_bit_cast(unsigned, fv[i]) : 0u; }
;             } else {
; #pragma unroll
;                 for (int i = 0; i < 32; ++i) kk[gI * 32 + i] = 0u;
;             }
;         }
.LBB0_723:
	s_cmp_gt_i32 s49, 32
	v_mov_b32_e32 v57, 0
	s_cselect_b64 s[6:7], -1, 0
	s_cmp_lt_i32 s49, 33
	v_mov_b32_e32 v94, 0
	v_mov_b32_e32 v96, 0
	v_mov_b32_e32 v98, 0
	v_mov_b32_e32 v100, 0
	v_mov_b32_e32 v102, 0
	v_mov_b32_e32 v103, 0
	v_mov_b32_e32 v104, 0
	v_mov_b32_e32 v105, 0
	v_mov_b32_e32 v106, 0
	v_mov_b32_e32 v107, 0
	v_mov_b32_e32 v108, 0
	v_mov_b32_e32 v109, 0
	v_mov_b32_e32 v110, 0
	v_mov_b32_e32 v111, 0
	v_mov_b32_e32 v112, 0
	v_mov_b32_e32 v113, 0
	v_mov_b32_e32 v114, 0
	v_mov_b32_e32 v115, 0
	v_mov_b32_e32 v116, 0
	v_mov_b32_e32 v117, 0
	v_mov_b32_e32 v118, 0
	v_mov_b32_e32 v119, 0
	v_mov_b32_e32 v120, 0
	v_mov_b32_e32 v121, 0
	v_mov_b32_e32 v122, 0
	v_mov_b32_e32 v123, 0
	v_mov_b32_e32 v124, 0
	v_mov_b32_e32 v125, 0
	v_mov_b32_e32 v127, 0
	v_mov_b32_e32 v131, 0
	v_mov_b32_e32 v133, 0
	v_mov_b32_e32 v135, 0
	s_cbranch_scc1 .LBB0_725
	v_readfirstlane_b32 s2, v0
	v_readfirstlane_b32 s3, v1
	v_lshlrev_b32_e32 v2, 2, v129
	s_nop 3
	s_add_u32 s2, s2, 0x2000
	s_addc_u32 s3, s3, 0
	s_add_i32 s4, s58, -2047
	s_nop 1
	global_load_dword v135, v2, s[2:3] sc1
	global_load_dword v133, v2, s[2:3] offset:256 sc1
	global_load_dword v131, v2, s[2:3] offset:512 sc1
	global_load_dword v127, v2, s[2:3] offset:768 sc1
	global_load_dword v125, v2, s[2:3] offset:1024 sc1
	global_load_dword v124, v2, s[2:3] offset:1280 sc1
	global_load_dword v123, v2, s[2:3] offset:1536 sc1
	global_load_dword v122, v2, s[2:3] offset:1792 sc1
	global_load_dword v121, v2, s[2:3] offset:2048 sc1
	global_load_dword v120, v2, s[2:3] offset:2304 sc1
	global_load_dword v119, v2, s[2:3] offset:2560 sc1
	global_load_dword v118, v2, s[2:3] offset:2816 sc1
	global_load_dword v117, v2, s[2:3] offset:3072 sc1
	global_load_dword v116, v2, s[2:3] offset:3328 sc1
	global_load_dword v115, v2, s[2:3] offset:3584 sc1
	global_load_dword v114, v2, s[2:3] offset:3840 sc1
	s_add_u32 s2, s2, 0x1000
	s_addc_u32 s3, s3, 0
	global_load_dword v113, v2, s[2:3] sc1
	global_load_dword v112, v2, s[2:3] offset:256 sc1
	global_load_dword v111, v2, s[2:3] offset:512 sc1
	global_load_dword v110, v2, s[2:3] offset:768 sc1
	global_load_dword v109, v2, s[2:3] offset:1024 sc1
	global_load_dword v108, v2, s[2:3] offset:1280 sc1
	global_load_dword v107, v2, s[2:3] offset:1536 sc1
	global_load_dword v106, v2, s[2:3] offset:1792 sc1
	global_load_dword v105, v2, s[2:3] offset:2048 sc1
	global_load_dword v104, v2, s[2:3] offset:2304 sc1
	global_load_dword v103, v2, s[2:3] offset:2560 sc1
	global_load_dword v102, v2, s[2:3] offset:2816 sc1
	global_load_dword v100, v2, s[2:3] offset:3072 sc1
	global_load_dword v98, v2, s[2:3] offset:3328 sc1
	global_load_dword v96, v2, s[2:3] offset:3584 sc1
	global_load_dword v94, v2, s[2:3] offset:3840 sc1
	v_cmp_gt_i32_e64 s[10:11], s4, v129
	s_sub_i32 s4, s4, 64
	v_cmp_gt_i32_e64 s[12:13], s4, v129
	s_sub_i32 s4, s4, 64
	v_cmp_gt_i32_e64 s[14:15], s4, v129
	s_sub_i32 s4, s4, 64
	v_cmp_gt_i32_e32 vcc, s4, v129
	s_sub_i32 s4, s4, 64
	s_waitcnt vmcnt(28)
	v_cndmask_b32_e64 v135, 0, v135, s[10:11]
	v_cndmask_b32_e64 v133, 0, v133, s[12:13]
	v_cndmask_b32_e64 v131, 0, v131, s[14:15]
	v_cndmask_b32_e32 v127, 0, v127, vcc
	v_cmp_gt_i32_e64 s[10:11], s4, v129
	s_sub_i32 s4, s4, 64
	v_cmp_gt_i32_e64 s[12:13], s4, v129
	s_sub_i32 s4, s4, 64
	v_cmp_gt_i32_e64 s[14:15], s4, v129
	s_sub_i32 s4, s4, 64
	v_cmp_gt_i32_e32 vcc, s4, v129
	s_sub_i32 s4, s4, 64
	s_waitcnt vmcnt(24)
	v_cndmask_b32_e64 v125, 0, v125, s[10:11]
	v_cndmask_b32_e64 v124, 0, v124, s[12:13]
	v_cndmask_b32_e64 v123, 0, v123, s[14:15]
	v_cndmask_b32_e32 v122, 0, v122, vcc
	v_cmp_gt_i32_e64 s[10:11], s4, v129
	s_sub_i32 s4, s4, 64
	v_cmp_gt_i32_e64 s[12:13], s4, v129
	s_sub_i32 s4, s4, 64
	v_cmp_gt_i32_e64 s[14:15], s4, v129
	s_sub_i32 s4, s4, 64
	v_cmp_gt_i32_e32 vcc, s4, v129
	s_sub_i32 s4, s4, 64
	s_waitcnt vmcnt(20)
	v_cndmask_b32_e64 v121, 0, v121, s[10:11]
	v_cndmask_b32_e64 v120, 0, v120, s[12:13]
	v_cndmask_b32_e64 v119, 0, v119, s[14:15]
	v_cndmask_b32_e32 v118, 0, v118, vcc
	v_cmp_gt_i32_e64 s[10:11], s4, v129
	s_sub_i32 s4, s4, 64
	v_cmp_gt_i32_e64 s[12:13], s4, v129
	s_sub_i32 s4, s4, 64
	v_cmp_gt_i32_e64 s[14:15], s4, v129
	s_sub_i32 s4, s4, 64
	v_cmp_gt_i32_e32 vcc, s4, v129
	s_sub_i32 s4, s4, 64
	s_waitcnt vmcnt(16)
	v_cndmask_b32_e64 v117, 0, v117, s[10:11]
	v_cndmask_b32_e64 v116, 0, v116, s[12:13]
	v_cndmask_b32_e64 v115, 0, v115, s[14:15]
	v_cndmask_b32_e32 v114, 0, v114, vcc
	v_cmp_gt_i32_e64 s[10:11], s4, v129
	s_sub_i32 s4, s4, 64
	v_cmp_gt_i32_e64 s[12:13], s4, v129
	s_sub_i32 s4, s4, 64
	v_cmp_gt_i32_e64 s[14:15], s4, v129
	s_sub_i32 s4, s4, 64
	v_cmp_gt_i32_e32 vcc, s4, v129
	s_sub_i32 s4, s4, 64
	s_waitcnt vmcnt(12)
	v_cndmask_b32_e64 v113, 0, v113, s[10:11]
	v_cndmask_b32_e64 v112, 0, v112, s[12:13]
	v_cndmask_b32_e64 v111, 0, v111, s[14:15]
	v_cndmask_b32_e32 v110, 0, v110, vcc
	v_cmp_gt_i32_e64 s[10:11], s4, v129
	s_sub_i32 s4, s4, 64
	v_cmp_gt_i32_e64 s[12:13], s4, v129
	s_sub_i32 s4, s4, 64
	v_cmp_gt_i32_e64 s[14:15], s4, v129
	s_sub_i32 s4, s4, 64
	v_cmp_gt_i32_e32 vcc, s4, v129
	s_sub_i32 s4, s4, 64
	s_waitcnt vmcnt(8)
	v_cndmask_b32_e64 v109, 0, v109, s[10:11]
	v_cndmask_b32_e64 v108, 0, v108, s[12:13]
	v_cndmask_b32_e64 v107, 0, v107, s[14:15]
	v_cndmask_b32_e32 v106, 0, v106, vcc
	v_cmp_gt_i32_e64 s[10:11], s4, v129
	s_sub_i32 s4, s4, 64
	v_cmp_gt_i32_e64 s[12:13], s4, v129
	s_sub_i32 s4, s4, 64
	v_cmp_gt_i32_e64 s[14:15], s4, v129
	s_sub_i32 s4, s4, 64
	v_cmp_gt_i32_e32 vcc, s4, v129
	s_sub_i32 s4, s4, 64
	s_waitcnt vmcnt(4)
	v_cndmask_b32_e64 v105, 0, v105, s[10:11]
	v_cndmask_b32_e64 v104, 0, v104, s[12:13]
	v_cndmask_b32_e64 v103, 0, v103, s[14:15]
	v_cndmask_b32_e32 v102, 0, v102, vcc
	v_cmp_gt_i32_e64 s[10:11], s4, v129
	s_sub_i32 s4, s4, 64
	v_cmp_gt_i32_e64 s[12:13], s4, v129
	s_sub_i32 s4, s4, 64
	v_cmp_gt_i32_e64 s[14:15], s4, v129
	s_sub_i32 s4, s4, 64
	v_cmp_gt_i32_e32 vcc, s4, v129
	s_sub_i32 s4, s4, 64
	s_waitcnt vmcnt(0)
	v_cndmask_b32_e64 v100, 0, v100, s[10:11]
	v_cndmask_b32_e64 v98, 0, v98, s[12:13]
	v_cndmask_b32_e64 v96, 0, v96, s[14:15]
	v_cndmask_b32_e32 v94, 0, v94, vcc
; __device__ __forceinline__ void dsa2_unit(LAS unsigned char* lds, const bf16* PROJ, const bf16* KIDX, const bf16* KVN, bf16* OLAT, float* sbuf, int b, int t0, int tid) {
;     ...
;         for (int repk = 0; repk < DUP_KK; ++repk)
; #pragma unroll
;         for (int gI = 0; gI < 4; ++gI) {
;             if (gI * 32 < nreg) {
;                 float fv[32];
; #pragma unroll
;                 for (int i = 0; i < 32; ++i) { const int key = lane + 64 * (gI * 32 + i); fv[i] = __hip_atomic_load(sr + (key < n ? key : n - 1), __ATOMIC_RELAXED, __HIP_MEMORY_SCOPE_AGENT); }
; #pragma unroll
;                 for (int i = 0; i < 32; ++i) { const int key = lane + 64 * (gI * 32 + i); kk[gI * 32 + i] = key < n ? __builtin_bit_cast(unsigned, fv[i]) : 0u; }
;             } else {
; #pragma unroll
;                 for (int i = 0; i < 32; ++i) kk[gI * 32 + i] = 0u;
;             }
;         }
.LBB0_725:
	s_cmp_gt_i32 s49, 64
	s_cselect_b64 s[18:19], -1, 0
	s_cmpk_lt_i32 s49, 0x41
	v_mov_b32_e32 v64, 0
	v_mov_b32_e32 v66, 0
	v_mov_b32_e32 v68, 0
	v_mov_b32_e32 v70, 0
	v_mov_b32_e32 v71, 0
	v_mov_b32_e32 v72, 0
	v_mov_b32_e32 v73, 0
	v_mov_b32_e32 v74, 0
	v_mov_b32_e32 v75, 0
	v_mov_b32_e32 v76, 0
	v_mov_b32_e32 v77, 0
	v_mov_b32_e32 v78, 0
	v_mov_b32_e32 v79, 0
	v_mov_b32_e32 v80, 0
	v_mov_b32_e32 v81, 0
	v_mov_b32_e32 v82, 0
	v_mov_b32_e32 v83, 0
	v_mov_b32_e32 v84, 0
	v_mov_b32_e32 v85, 0
	v_mov_b32_e32 v86, 0
	v_mov_b32_e32 v87, 0
	v_mov_b32_e32 v88, 0
	v_mov_b32_e32 v89, 0
	v_mov_b32_e32 v90, 0
	v_mov_b32_e32 v91, 0
	v_mov_b32_e32 v92, 0
	v_mov_b32_e32 v93, 0
	v_mov_b32_e32 v95, 0
	v_mov_b32_e32 v97, 0
	v_mov_b32_e32 v99, 0
	v_mov_b32_e32 v101, 0
	s_cbranch_scc1 .LBB0_727
	v_readfirstlane_b32 s2, v0
	v_readfirstlane_b32 s3, v1
	v_lshlrev_b32_e32 v2, 2, v129
	s_nop 3
	s_add_u32 s2, s2, 0x4000
	s_addc_u32 s3, s3, 0
	s_add_i32 s4, s58, -4095
	s_nop 1
	global_load_dword v101, v2, s[2:3] sc1
	global_load_dword v99, v2, s[2:3] offset:256 sc1
	global_load_dword v97, v2, s[2:3] offset:512 sc1
	global_load_dword v95, v2, s[2:3] offset:768 sc1
	global_load_dword v93, v2, s[2:3] offset:1024 sc1
	global_load_dword v92, v2, s[2:3] offset:1280 sc1
	global_load_dword v91, v2, s[2:3] offset:1536 sc1
	global_load_dword v90, v2, s[2:3] offset:1792 sc1
	global_load_dword v89, v2, s[2:3] offset:2048 sc1
	global_load_dword v88, v2, s[2:3] offset:2304 sc1
	global_load_dword v87, v2, s[2:3] offset:2560 sc1
	global_load_dword v86, v2, s[2:3] offset:2816 sc1
	global_load_dword v85, v2, s[2:3] offset:3072 sc1
	global_load_dword v84, v2, s[2:3] offset:3328 sc1
	global_load_dword v83, v2, s[2:3] offset:3584 sc1
	global_load_dword v82, v2, s[2:3] offset:3840 sc1
	s_add_u32 s2, s2, 0x1000
	s_addc_u32 s3, s3, 0
	global_load_dword v81, v2, s[2:3] sc1
	global_load_dword v80, v2, s[2:3] offset:256 sc1
	global_load_dword v79, v2, s[2:3] offset:512 sc1
	global_load_dword v78, v2, s[2:3] offset:768 sc1
	global_load_dword v77, v2, s[2:3] offset:1024 sc1
	global_load_dword v76, v2, s[2:3] offset:1280 sc1
	global_load_dword v75, v2, s[2:3] offset:1536 sc1
	global_load_dword v74, v2, s[2:3] offset:1792 sc1
	global_load_dword v73, v2, s[2:3] offset:2048 sc1
	global_load_dword v72, v2, s[2:3] offset:2304 sc1
	global_load_dword v71, v2, s[2:3] offset:2560 sc1
	global_load_dword v70, v2, s[2:3] offset:2816 sc1
	global_load_dword v68, v2, s[2:3] offset:3072 sc1
	global_load_dword v66, v2, s[2:3] offset:3328 sc1
	global_load_dword v64, v2, s[2:3] offset:3584 sc1
	global_load_dword v57, v2, s[2:3] offset:3840 sc1
	v_cmp_gt_i32_e64 s[10:11], s4, v129
	s_sub_i32 s4, s4, 64
	v_cmp_gt_i32_e64 s[12:13], s4, v129
	s_sub_i32 s4, s4, 64
	v_cmp_gt_i32_e64 s[14:15], s4, v129
	s_sub_i32 s4, s4, 64
	v_cmp_gt_i32_e32 vcc, s4, v129
	s_sub_i32 s4, s4, 64
	s_waitcnt vmcnt(28)
	v_cndmask_b32_e64 v101, 0, v101, s[10:11]
	v_cndmask_b32_e64 v99, 0, v99, s[12:13]
	v_cndmask_b32_e64 v97, 0, v97, s[14:15]
	v_cndmask_b32_e32 v95, 0, v95, vcc
	v_cmp_gt_i32_e64 s[10:11], s4, v129
	s_sub_i32 s4, s4, 64
	v_cmp_gt_i32_e64 s[12:13], s4, v129
	s_sub_i32 s4, s4, 64
	v_cmp_gt_i32_e64 s[14:15], s4, v129
	s_sub_i32 s4, s4, 64
	v_cmp_gt_i32_e32 vcc, s4, v129
	s_sub_i32 s4, s4, 64
	s_waitcnt vmcnt(24)
	v_cndmask_b32_e64 v93, 0, v93, s[10:11]
	v_cndmask_b32_e64 v92, 0, v92, s[12:13]
	v_cndmask_b32_e64 v91, 0, v91, s[14:15]
	v_cndmask_b32_e32 v90, 0, v90, vcc
	v_cmp_gt_i32_e64 s[10:11], s4, v129
	s_sub_i32 s4, s4, 64
	v_cmp_gt_i32_e64 s[12:13], s4, v129
	s_sub_i32 s4, s4, 64
	v_cmp_gt_i32_e64 s[14:15], s4, v129
	s_sub_i32 s4, s4, 64
	v_cmp_gt_i32_e32 vcc, s4, v129
	s_sub_i32 s4, s4, 64
	s_waitcnt vmcnt(20)
	v_cndmask_b32_e64 v89, 0, v89, s[10:11]
	v_cndmask_b32_e64 v88, 0, v88, s[12:13]
	v_cndmask_b32_e64 v87, 0, v87, s[14:15]
	v_cndmask_b32_e32 v86, 0, v86, vcc
	v_cmp_gt_i32_e64 s[10:11], s4, v129
	s_sub_i32 s4, s4, 64
	v_cmp_gt_i32_e64 s[12:13], s4, v129
	s_sub_i32 s4, s4, 64
	v_cmp_gt_i32_e64 s[14:15], s4, v129
	s_sub_i32 s4, s4, 64
	v_cmp_gt_i32_e32 vcc, s4, v129
	s_sub_i32 s4, s4, 64
	s_waitcnt vmcnt(16)
	v_cndmask_b32_e64 v85, 0, v85, s[10:11]
	v_cndmask_b32_e64 v84, 0, v84, s[12:13]
	v_cndmask_b32_e64 v83, 0, v83, s[14:15]
	v_cndmask_b32_e32 v82, 0, v82, vcc
	v_cmp_gt_i32_e64 s[10:11], s4, v129
	s_sub_i32 s4, s4, 64
	v_cmp_gt_i32_e64 s[12:13], s4, v129
	s_sub_i32 s4, s4, 64
	v_cmp_gt_i32_e64 s[14:15], s4, v129
	s_sub_i32 s4, s4, 64
	v_cmp_gt_i32_e32 vcc, s4, v129
	s_sub_i32 s4, s4, 64
	s_waitcnt vmcnt(12)
	v_cndmask_b32_e64 v81, 0, v81, s[10:11]
	v_cndmask_b32_e64 v80, 0, v80, s[12:13]
	v_cndmask_b32_e64 v79, 0, v79, s[14:15]
	v_cndmask_b32_e32 v78, 0, v78, vcc
	v_cmp_gt_i32_e64 s[10:11], s4, v129
	s_sub_i32 s4, s4, 64
	v_cmp_gt_i32_e64 s[12:13], s4, v129
	s_sub_i32 s4, s4, 64
	v_cmp_gt_i32_e64 s[14:15], s4, v129
	s_sub_i32 s4, s4, 64
	v_cmp_gt_i32_e32 vcc, s4, v129
	s_sub_i32 s4, s4, 64
	s_waitcnt vmcnt(8)
	v_cndmask_b32_e64 v77, 0, v77, s[10:11]
	v_cndmask_b32_e64 v76, 0, v76, s[12:13]
	v_cndmask_b32_e64 v75, 0, v75, s[14:15]
	v_cndmask_b32_e32 v74, 0, v74, vcc
	v_cmp_gt_i32_e64 s[10:11], s4, v129
	s_sub_i32 s4, s4, 64
	v_cmp_gt_i32_e64 s[12:13], s4, v129
	s_sub_i32 s4, s4, 64
	v_cmp_gt_i32_e64 s[14:15], s4, v129
	s_sub_i32 s4, s4, 64
	v_cmp_gt_i32_e32 vcc, s4, v129
	s_sub_i32 s4, s4, 64
	s_waitcnt vmcnt(4)
	v_cndmask_b32_e64 v73, 0, v73, s[10:11]
	v_cndmask_b32_e64 v72, 0, v72, s[12:13]
	v_cndmask_b32_e64 v71, 0, v71, s[14:15]
	v_cndmask_b32_e32 v70, 0, v70, vcc
	v_cmp_gt_i32_e64 s[10:11], s4, v129
	s_sub_i32 s4, s4, 64
	v_cmp_gt_i32_e64 s[12:13], s4, v129
	s_sub_i32 s4, s4, 64
	v_cmp_gt_i32_e64 s[14:15], s4, v129
	s_sub_i32 s4, s4, 64
	v_cmp_gt_i32_e32 vcc, s4, v129
	s_sub_i32 s4, s4, 64
	s_waitcnt vmcnt(0)
	v_cndmask_b32_e64 v68, 0, v68, s[10:11]
	v_cndmask_b32_e64 v66, 0, v66, s[12:13]
	v_cndmask_b32_e64 v64, 0, v64, s[14:15]
	v_cndmask_b32_e32 v57, 0, v57, vcc
; __device__ __forceinline__ void dsa2_unit(LAS unsigned char* lds, const bf16* PROJ, const bf16* KIDX, const bf16* KVN, bf16* OLAT, float* sbuf, int b, int t0, int tid) {
;     ...
;         for (int repk = 0; repk < DUP_KK; ++repk)
; #pragma unroll
;         for (int gI = 0; gI < 4; ++gI) {
;             if (gI * 32 < nreg) {
;                 float fv[32];
; #pragma unroll
;                 for (int i = 0; i < 32; ++i) { const int key = lane + 64 * (gI * 32 + i); fv[i] = __hip_atomic_load(sr + (key < n ? key : n - 1), __ATOMIC_RELAXED, __HIP_MEMORY_SCOPE_AGENT); }
; #pragma unroll
;                 for (int i = 0; i < 32; ++i) { const int key = lane + 64 * (gI * 32 + i); kk[gI * 32 + i] = key < n ? __builtin_bit_cast(unsigned, fv[i]) : 0u; }
;             } else {
; #pragma unroll
;                 for (int i = 0; i < 32; ++i) kk[gI * 32 + i] = 0u;
;             }
;         }
.LBB0_727:
	s_cmpk_gt_i32 s49, 0x60
	v_mov_b32_e32 v32, 0
	s_cselect_b64 s[16:17], -1, 0
	s_cmpk_lt_i32 s49, 0x61
	v_mov_b32_e32 v35, 0
	v_mov_b32_e32 v36, 0
	v_mov_b32_e32 v37, 0
	v_mov_b32_e32 v38, 0
	v_mov_b32_e32 v39, 0
	v_mov_b32_e32 v40, 0
	v_mov_b32_e32 v41, 0
	v_mov_b32_e32 v42, 0
	v_mov_b32_e32 v43, 0
	v_mov_b32_e32 v44, 0
	v_mov_b32_e32 v45, 0
	v_mov_b32_e32 v46, 0
	v_mov_b32_e32 v47, 0
	v_mov_b32_e32 v48, 0
	v_mov_b32_e32 v49, 0
	v_mov_b32_e32 v50, 0
	v_mov_b32_e32 v51, 0
	v_mov_b32_e32 v52, 0
	v_mov_b32_e32 v53, 0
	v_mov_b32_e32 v54, 0
	v_mov_b32_e32 v55, 0
	v_mov_b32_e32 v56, 0
	v_mov_b32_e32 v58, 0
	v_mov_b32_e32 v59, 0
	v_mov_b32_e32 v60, 0
	v_mov_b32_e32 v61, 0
	v_mov_b32_e32 v62, 0
	v_mov_b32_e32 v63, 0
	v_mov_b32_e32 v65, 0
	v_mov_b32_e32 v67, 0
	v_mov_b32_e32 v69, 0
	s_cbranch_scc1 .LBB0_729
	v_readfirstlane_b32 s2, v0
	v_readfirstlane_b32 s3, v1
	v_lshlrev_b32_e32 v2, 2, v129
	s_nop 3
	s_add_u32 s2, s2, 0x6000
	s_addc_u32 s3, s3, 0
	s_add_i32 s4, s58, -6143
	s_nop 1
	global_load_dword v69, v2, s[2:3] sc1
	global_load_dword v67, v2, s[2:3] offset:256 sc1
	global_load_dword v65, v2, s[2:3] offset:512 sc1
	global_load_dword v63, v2, s[2:3] offset:768 sc1
	global_load_dword v62, v2, s[2:3] offset:1024 sc1
	global_load_dword v61, v2, s[2:3] offset:1280 sc1
	global_load_dword v60, v2, s[2:3] offset:1536 sc1
	global_load_dword v59, v2, s[2:3] offset:1792 sc1
	global_load_dword v58, v2, s[2:3] offset:2048 sc1
	global_load_dword v56, v2, s[2:3] offset:2304 sc1
	global_load_dword v55, v2, s[2:3] offset:2560 sc1
	global_load_dword v54, v2, s[2:3] offset:2816 sc1
	global_load_dword v53, v2, s[2:3] offset:3072 sc1
	global_load_dword v52, v2, s[2:3] offset:3328 sc1
	global_load_dword v51, v2, s[2:3] offset:3584 sc1
	global_load_dword v50, v2, s[2:3] offset:3840 sc1
	s_add_u32 s2, s2, 0x1000
	s_addc_u32 s3, s3, 0
	global_load_dword v49, v2, s[2:3] sc1
	global_load_dword v48, v2, s[2:3] offset:256 sc1
	global_load_dword v47, v2, s[2:3] offset:512 sc1
	global_load_dword v46, v2, s[2:3] offset:768 sc1
	global_load_dword v45, v2, s[2:3] offset:1024 sc1
	global_load_dword v44, v2, s[2:3] offset:1280 sc1
	global_load_dword v43, v2, s[2:3] offset:1536 sc1
	global_load_dword v42, v2, s[2:3] offset:1792 sc1
	global_load_dword v41, v2, s[2:3] offset:2048 sc1
	global_load_dword v40, v2, s[2:3] offset:2304 sc1
	global_load_dword v39, v2, s[2:3] offset:2560 sc1
	global_load_dword v38, v2, s[2:3] offset:2816 sc1
	global_load_dword v37, v2, s[2:3] offset:3072 sc1
	global_load_dword v36, v2, s[2:3] offset:3328 sc1
	global_load_dword v35, v2, s[2:3] offset:3584 sc1
	global_load_dword v32, v2, s[2:3] offset:3840 sc1
	v_cmp_gt_i32_e64 s[10:11], s4, v129
	s_sub_i32 s4, s4, 64
	v_cmp_gt_i32_e64 s[12:13], s4, v129
	s_sub_i32 s4, s4, 64
	v_cmp_gt_i32_e64 s[14:15], s4, v129
	s_sub_i32 s4, s4, 64
	v_cmp_gt_i32_e32 vcc, s4, v129
	s_sub_i32 s4, s4, 64
	s_waitcnt vmcnt(28)
	v_cndmask_b32_e64 v69, 0, v69, s[10:11]
	v_cndmask_b32_e64 v67, 0, v67, s[12:13]
	v_cndmask_b32_e64 v65, 0, v65, s[14:15]
	v_cndmask_b32_e32 v63, 0, v63, vcc
	v_cmp_gt_i32_e64 s[10:11], s4, v129
	s_sub_i32 s4, s4, 64
	v_cmp_gt_i32_e64 s[12:13], s4, v129
	s_sub_i32 s4, s4, 64
	v_cmp_gt_i32_e64 s[14:15], s4, v129
	s_sub_i32 s4, s4, 64
	v_cmp_gt_i32_e32 vcc, s4, v129
	s_sub_i32 s4, s4, 64
	s_waitcnt vmcnt(24)
	v_cndmask_b32_e64 v62, 0, v62, s[10:11]
	v_cndmask_b32_e64 v61, 0, v61, s[12:13]
	v_cndmask_b32_e64 v60, 0, v60, s[14:15]
	v_cndmask_b32_e32 v59, 0, v59, vcc
	v_cmp_gt_i32_e64 s[10:11], s4, v129
	s_sub_i32 s4, s4, 64
	v_cmp_gt_i32_e64 s[12:13], s4, v129
	s_sub_i32 s4, s4, 64
	v_cmp_gt_i32_e64 s[14:15], s4, v129
	s_sub_i32 s4, s4, 64
	v_cmp_gt_i32_e32 vcc, s4, v129
	s_sub_i32 s4, s4, 64
	s_waitcnt vmcnt(20)
	v_cndmask_b32_e64 v58, 0, v58, s[10:11]
	v_cndmask_b32_e64 v56, 0, v56, s[12:13]
	v_cndmask_b32_e64 v55, 0, v55, s[14:15]
	v_cndmask_b32_e32 v54, 0, v54, vcc
	v_cmp_gt_i32_e64 s[10:11], s4, v129
	s_sub_i32 s4, s4, 64
	v_cmp_gt_i32_e64 s[12:13], s4, v129
	s_sub_i32 s4, s4, 64
	v_cmp_gt_i32_e64 s[14:15], s4, v129
	s_sub_i32 s4, s4, 64
	v_cmp_gt_i32_e32 vcc, s4, v129
	s_sub_i32 s4, s4, 64
	s_waitcnt vmcnt(16)
	v_cndmask_b32_e64 v53, 0, v53, s[10:11]
	v_cndmask_b32_e64 v52, 0, v52, s[12:13]
	v_cndmask_b32_e64 v51, 0, v51, s[14:15]
	v_cndmask_b32_e32 v50, 0, v50, vcc
	v_cmp_gt_i32_e64 s[10:11], s4, v129
	s_sub_i32 s4, s4, 64
	v_cmp_gt_i32_e64 s[12:13], s4, v129
	s_sub_i32 s4, s4, 64
	v_cmp_gt_i32_e64 s[14:15], s4, v129
	s_sub_i32 s4, s4, 64
	v_cmp_gt_i32_e32 vcc, s4, v129
	s_sub_i32 s4, s4, 64
	s_waitcnt vmcnt(12)
	v_cndmask_b32_e64 v49, 0, v49, s[10:11]
	v_cndmask_b32_e64 v48, 0, v48, s[12:13]
	v_cndmask_b32_e64 v47, 0, v47, s[14:15]
	v_cndmask_b32_e32 v46, 0, v46, vcc
	v_cmp_gt_i32_e64 s[10:11], s4, v129
	s_sub_i32 s4, s4, 64
	v_cmp_gt_i32_e64 s[12:13], s4, v129
	s_sub_i32 s4, s4, 64
	v_cmp_gt_i32_e64 s[14:15], s4, v129
	s_sub_i32 s4, s4, 64
	v_cmp_gt_i32_e32 vcc, s4, v129
	s_sub_i32 s4, s4, 64
	s_waitcnt vmcnt(8)
	v_cndmask_b32_e64 v45, 0, v45, s[10:11]
	v_cndmask_b32_e64 v44, 0, v44, s[12:13]
	v_cndmask_b32_e64 v43, 0, v43, s[14:15]
	v_cndmask_b32_e32 v42, 0, v42, vcc
	v_cmp_gt_i32_e64 s[10:11], s4, v129
	s_sub_i32 s4, s4, 64
	v_cmp_gt_i32_e64 s[12:13], s4, v129
	s_sub_i32 s4, s4, 64
	v_cmp_gt_i32_e64 s[14:15], s4, v129
	s_sub_i32 s4, s4, 64
	v_cmp_gt_i32_e32 vcc, s4, v129
	s_sub_i32 s4, s4, 64
	s_waitcnt vmcnt(4)
	v_cndmask_b32_e64 v41, 0, v41, s[10:11]
	v_cndmask_b32_e64 v40, 0, v40, s[12:13]
	v_cndmask_b32_e64 v39, 0, v39, s[14:15]
	v_cndmask_b32_e32 v38, 0, v38, vcc
	v_cmp_gt_i32_e64 s[10:11], s4, v129
	s_sub_i32 s4, s4, 64
	v_cmp_gt_i32_e64 s[12:13], s4, v129
	s_sub_i32 s4, s4, 64
	v_cmp_gt_i32_e64 s[14:15], s4, v129
	s_sub_i32 s4, s4, 64
	v_cmp_gt_i32_e32 vcc, s4, v129
	s_sub_i32 s4, s4, 64
	s_waitcnt vmcnt(0)
	v_cndmask_b32_e64 v37, 0, v37, s[10:11]
	v_cndmask_b32_e64 v36, 0, v36, s[12:13]
	v_cndmask_b32_e64 v35, 0, v35, s[14:15]
	v_cndmask_b32_e32 v32, 0, v32, vcc
